# MLA attention: the softmax row-sum exchange between wave halves also by v_permlane32_swap (no ds_bpermute left in the tile loop)
# speedup vs baseline: 1.0084x; 1.0033x over previous
.LBB0_829:
	v_mul_f32_e32 v151, 0x3e16c740, v2
	v_fma_f32 v36, v36, s3, -v151
	v_exp_f32_e32 v154, v36
	v_fma_f32 v36, v53, s3, -v151
	v_fma_f32 v52, v52, s3, -v151
	v_exp_f32_e32 v155, v36
	v_fma_f32 v36, v37, s3, -v151
	v_exp_f32_e32 v153, v52
	v_exp_f32_e32 v156, v36
	v_fma_f32 v36, v54, s3, -v151
	v_exp_f32_e32 v157, v36
	v_fma_f32 v36, v38, s3, -v151
	v_fma_f32 v38, v55, s3, -v151
	v_exp_f32_e32 v158, v36
	v_exp_f32_e32 v159, v38
	v_fma_f32 v38, v39, s3, -v151
	v_exp_f32_e32 v160, v38
	v_add_f32_e32 v52, v153, v154
	v_add_f32_e32 v36, 0, v52
	v_add_f32_e32 v37, v155, v156
	v_add_f32_e32 v36, v37, v36
	v_add_f32_e32 v37, v157, v158
	v_fma_f32 v38, v56, s3, -v151
	v_add_f32_e32 v36, v37, v36
	v_add_f32_e32 v37, v159, v160
	v_exp_f32_e32 v161, v38
	v_fma_f32 v38, v40, s3, -v151
	v_add_f32_e32 v40, v37, v36
	v_fma_f32 v36, v57, s3, -v151
	v_exp_f32_e32 v163, v36
	v_fma_f32 v36, v41, s3, -v151
	v_exp_f32_e32 v164, v36
	v_fma_f32 v36, v58, s3, -v151
	v_exp_f32_e32 v162, v38
	v_exp_f32_e32 v37, v36
	v_fma_f32 v36, v42, s3, -v151
	v_exp_f32_e32 v39, v36
	v_fma_f32 v36, v59, s3, -v151
	v_fma_f32 v38, v43, s3, -v151
	v_exp_f32_e32 v36, v36
	v_exp_f32_e32 v38, v38
	v_add_f32_e32 v52, v161, v162
	v_add_f32_e32 v40, v52, v40
	v_add_f32_e32 v41, v163, v164
	v_add_f32_e32 v42, v41, v40
	v_pk_add_f32 v[40:41], v[36:37], v[38:39]
	v_add_f32_e32 v41, v41, v42
	v_fma_f32 v42, v60, s3, -v151
	v_exp_f32_e32 v43, v42
	v_fma_f32 v42, v44, s3, -v151
	v_exp_f32_e32 v167, v42
	v_fma_f32 v42, v61, s3, -v151
	v_fma_f32 v44, v45, s3, -v151
	v_exp_f32_e32 v42, v42
	v_exp_f32_e32 v166, v44
	v_add_f32_e32 v44, v40, v41
	s_andn2_b64 vcc, exec, s[18:19]
	v_pk_add_f32 v[40:41], v[42:43], v[166:167]
	v_add_f32_e32 v41, v41, v44
	v_fma_f32 v44, v62, s3, -v151
	v_exp_f32_e32 v169, v44
	v_fma_f32 v44, v46, s3, -v151
	v_exp_f32_e32 v55, v44
	v_fma_f32 v44, v63, s3, -v151
	v_fma_f32 v46, v47, s3, -v151
	v_exp_f32_e32 v168, v44
	v_exp_f32_e32 v54, v46
	v_add_f32_e32 v46, v40, v41
	v_pk_add_f32 v[40:41], v[168:169], v[54:55]
	v_pk_mov_b32 v[54:55], v[54:55], v[54:55] op_sel:[1,0]
	v_add_f32_e32 v41, v41, v46
	v_fma_f32 v46, v64, s3, -v151
	v_exp_f32_e32 v47, v46
	v_fma_f32 v46, v48, s3, -v151
	v_exp_f32_e32 v171, v46
	v_fma_f32 v46, v65, s3, -v151
	v_fma_f32 v48, v49, s3, -v151
	v_exp_f32_e32 v46, v46
	v_exp_f32_e32 v170, v48
	v_add_f32_e32 v44, v40, v41
	v_fma_f32 v48, v51, s3, -v151
	v_exp_f32_e32 v172, v48
	v_pk_add_f32 v[40:41], v[46:47], v[170:171]
	v_add_f32_e32 v41, v41, v44
	v_fma_f32 v44, v66, s3, -v151
	v_exp_f32_e32 v175, v44
	v_fma_f32 v44, v50, s3, -v151
	v_exp_f32_e32 v173, v44
	v_fma_f32 v44, v67, s3, -v151
	v_exp_f32_e32 v174, v44
	v_add_f32_e32 v50, v40, v41
	v_pk_add_f32 v[40:41], v[174:175], v[172:173]
	v_add_f32_e32 v41, v41, v50
	v_add_f32_e32 v52, v40, v41
	v_mov_b32_e32 v53, v52
	s_nop 3
	v_permlane32_swap_b32_e32 v52, v53
	s_nop 1
	v_cvt_pk_bf16_f32 v48, v153, v155
	v_cvt_pk_bf16_f32 v49, v157, v159
	v_cvt_pk_bf16_f32 v50, v161, v163
	v_cvt_pk_bf16_f32 v51, v37, v36
	v_cvt_pk_bf16_f32 v44, v43, v42
	v_cvt_pk_bf16_f32 v45, v169, v168
	v_cvt_pk_bf16_f32 v46, v47, v46
	v_cvt_pk_bf16_f32 v47, v175, v174
	v_cvt_pk_bf16_f32 v40, v154, v156
	v_cvt_pk_bf16_f32 v41, v158, v160
	v_cvt_pk_bf16_f32 v42, v162, v164
	v_cvt_pk_bf16_f32 v43, v39, v38
	v_cvt_pk_bf16_f32 v36, v167, v166
	v_cvt_pk_bf16_f32 v37, v54, v55
	v_cvt_pk_bf16_f32 v38, v171, v170
	v_cvt_pk_bf16_f32 v39, v173, v172
	s_mov_b64 s[12:13], -1
	s_cbranch_vccnz .LBB0_832
	v_add3_u32 v58, s4, v146, v125
	v_add_u32_e32 v59, 0x3000, v58
	ds_read2_b64 v[54:57], v59 offset0:128 offset1:130
	v_add_u32_e32 v58, 0x4000, v58
	s_mov_b64 s[12:13], 0
	s_waitcnt lgkmcnt(0)
	v_mfma_f32_32x32x16_bf16 v[20:35], v[54:57], v[48:51], v[20:35]
	ds_read2_b64 v[54:57], v58 offset0:160 offset1:162
	s_waitcnt lgkmcnt(0)
	v_mfma_f32_32x32x16_bf16 v[4:19], v[54:57], v[48:51], v[4:19]
	ds_read2_b64 v[54:57], v59 offset0:132 offset1:134
	s_waitcnt lgkmcnt(0)
	v_mfma_f32_32x32x16_bf16 v[20:35], v[54:57], v[44:47], v[20:35]
	ds_read2_b64 v[54:57], v58 offset0:164 offset1:166
	s_waitcnt lgkmcnt(0)
	v_mfma_f32_32x32x16_bf16 v[4:19], v[54:57], v[44:47], v[4:19]
	ds_read2_b64 v[54:57], v59 offset0:136 offset1:138
	s_waitcnt lgkmcnt(0)
	v_mfma_f32_32x32x16_bf16 v[20:35], v[54:57], v[40:43], v[20:35]
	ds_read2_b64 v[54:57], v58 offset0:168 offset1:170
	s_waitcnt lgkmcnt(0)
	v_mfma_f32_32x32x16_bf16 v[4:19], v[54:57], v[40:43], v[4:19]
	ds_read2_b64 v[54:57], v59 offset0:140 offset1:142
	s_waitcnt lgkmcnt(0)
	v_mfma_f32_32x32x16_bf16 v[20:35], v[54:57], v[36:39], v[20:35]
	ds_read2_b64 v[54:57], v58 offset0:172 offset1:174
	s_waitcnt lgkmcnt(0)
	v_mfma_f32_32x32x16_bf16 v[4:19], v[54:57], v[36:39], v[4:19]
	s_branch .LBB0_833

.LBB0_845:
	v_mul_f32_e32 v2, 0x3e16c740, v69
	v_fma_f32 v36, v36, s3, -v2
	v_exp_f32_e32 v70, v36
	v_fma_f32 v36, v53, s3, -v2
	v_fma_f32 v52, v52, s3, -v2
	v_exp_f32_e32 v71, v36
	v_fma_f32 v36, v37, s3, -v2
	v_exp_f32_e32 v69, v52
	v_exp_f32_e32 v72, v36
	v_fma_f32 v36, v54, s3, -v2
	v_exp_f32_e32 v73, v36
	v_fma_f32 v36, v38, s3, -v2
	v_fma_f32 v38, v55, s3, -v2
	v_exp_f32_e32 v74, v36
	v_exp_f32_e32 v75, v38
	v_fma_f32 v38, v39, s3, -v2
	v_exp_f32_e32 v76, v38
	v_add_f32_e32 v52, v69, v70
	v_add_f32_e32 v36, 0, v52
	v_add_f32_e32 v37, v71, v72
	v_add_f32_e32 v36, v37, v36
	v_add_f32_e32 v37, v73, v74
	v_fma_f32 v38, v56, s3, -v2
	v_add_f32_e32 v36, v37, v36
	v_add_f32_e32 v37, v75, v76
	v_exp_f32_e32 v77, v38
	v_fma_f32 v38, v40, s3, -v2
	v_add_f32_e32 v40, v37, v36
	v_fma_f32 v36, v57, s3, -v2
	v_exp_f32_e32 v79, v36
	v_fma_f32 v36, v41, s3, -v2
	v_exp_f32_e32 v80, v36
	v_fma_f32 v36, v58, s3, -v2
	v_exp_f32_e32 v78, v38
	v_exp_f32_e32 v37, v36
	v_fma_f32 v36, v42, s3, -v2
	v_exp_f32_e32 v39, v36
	v_fma_f32 v36, v59, s3, -v2
	v_fma_f32 v38, v43, s3, -v2
	v_exp_f32_e32 v36, v36
	v_exp_f32_e32 v38, v38
	v_add_f32_e32 v52, v77, v78
	v_add_f32_e32 v40, v52, v40
	v_add_f32_e32 v41, v79, v80
	v_add_f32_e32 v42, v41, v40
	v_pk_add_f32 v[40:41], v[36:37], v[38:39]
	v_add_f32_e32 v41, v41, v42
	v_fma_f32 v42, v60, s3, -v2
	v_exp_f32_e32 v43, v42
	v_fma_f32 v42, v44, s3, -v2
	v_exp_f32_e32 v177, v42
	v_fma_f32 v42, v61, s3, -v2
	v_fma_f32 v44, v45, s3, -v2
	v_exp_f32_e32 v42, v42
	v_exp_f32_e32 v176, v44
	v_add_f32_e32 v44, v40, v41
	s_andn2_b64 vcc, exec, s[18:19]
	v_pk_add_f32 v[40:41], v[42:43], v[176:177]
	v_add_f32_e32 v41, v41, v44
	v_fma_f32 v44, v62, s3, -v2
	v_exp_f32_e32 v179, v44
	v_fma_f32 v44, v46, s3, -v2
	v_exp_f32_e32 v55, v44
	v_fma_f32 v44, v63, s3, -v2
	v_fma_f32 v46, v47, s3, -v2
	v_exp_f32_e32 v178, v44
	v_exp_f32_e32 v54, v46
	v_add_f32_e32 v46, v40, v41
	v_pk_add_f32 v[40:41], v[178:179], v[54:55]
	v_pk_mov_b32 v[54:55], v[54:55], v[54:55] op_sel:[1,0]
	v_add_f32_e32 v41, v41, v46
	v_fma_f32 v46, v64, s3, -v2
	v_exp_f32_e32 v47, v46
	v_fma_f32 v46, v48, s3, -v2
	v_exp_f32_e32 v181, v46
	v_fma_f32 v46, v65, s3, -v2
	v_fma_f32 v48, v49, s3, -v2
	v_exp_f32_e32 v46, v46
	v_exp_f32_e32 v180, v48
	v_add_f32_e32 v44, v40, v41
	s_mov_b64 s[4:5], -1
	v_pk_add_f32 v[40:41], v[46:47], v[180:181]
	s_nop 0
	v_add_f32_e32 v41, v41, v44
	v_fma_f32 v44, v66, s3, -v2
	v_exp_f32_e32 v183, v44
	v_fma_f32 v44, v50, s3, -v2
	v_exp_f32_e32 v185, v44
	v_fma_f32 v44, v67, s3, -v2
	v_fma_f32 v2, v51, s3, -v2
	v_exp_f32_e32 v182, v44
	v_exp_f32_e32 v184, v2
	v_add_f32_e32 v2, v40, v41
	v_pk_add_f32 v[40:41], v[182:183], v[184:185]
	v_add_f32_e32 v2, v41, v2
	v_add_f32_e32 v2, v40, v2
	v_mov_b32_e32 v52, v2
	s_nop 3
	v_permlane32_swap_b32_e32 v2, v52
	s_nop 1
	v_cvt_pk_bf16_f32 v48, v69, v71
	v_cvt_pk_bf16_f32 v49, v73, v75
	v_cvt_pk_bf16_f32 v50, v77, v79
	v_cvt_pk_bf16_f32 v51, v37, v36
	v_cvt_pk_bf16_f32 v44, v43, v42
	v_cvt_pk_bf16_f32 v45, v179, v178
	v_cvt_pk_bf16_f32 v46, v47, v46
	v_cvt_pk_bf16_f32 v47, v183, v182
	v_cvt_pk_bf16_f32 v40, v70, v72
	v_cvt_pk_bf16_f32 v41, v74, v76
	v_cvt_pk_bf16_f32 v42, v78, v80
	v_cvt_pk_bf16_f32 v43, v39, v38
	v_cvt_pk_bf16_f32 v36, v177, v176
	v_cvt_pk_bf16_f32 v37, v54, v55
	v_cvt_pk_bf16_f32 v38, v181, v180
	v_cvt_pk_bf16_f32 v39, v185, v184
	s_cbranch_vccnz .LBB0_847
	v_add3_u32 v53, s42, v146, v125
	v_add_u32_e32 v58, 0x3000, v53
	ds_read2_b64 v[54:57], v58 offset0:128 offset1:130
	v_add_u32_e32 v53, 0x4000, v53
	s_mov_b64 s[4:5], 0
	s_waitcnt lgkmcnt(0)
	v_mfma_f32_32x32x16_bf16 v[20:35], v[54:57], v[48:51], v[20:35]
	ds_read2_b64 v[54:57], v53 offset0:160 offset1:162
	s_waitcnt lgkmcnt(0)
	v_mfma_f32_32x32x16_bf16 v[4:19], v[54:57], v[48:51], v[4:19]
	ds_read2_b64 v[54:57], v58 offset0:132 offset1:134
	s_waitcnt lgkmcnt(0)
	v_mfma_f32_32x32x16_bf16 v[20:35], v[54:57], v[44:47], v[20:35]
	ds_read2_b64 v[54:57], v53 offset0:164 offset1:166
	s_waitcnt lgkmcnt(0)
	v_mfma_f32_32x32x16_bf16 v[4:19], v[54:57], v[44:47], v[4:19]
	ds_read2_b64 v[54:57], v58 offset0:136 offset1:138
	s_waitcnt lgkmcnt(0)
	v_mfma_f32_32x32x16_bf16 v[20:35], v[54:57], v[40:43], v[20:35]
	ds_read2_b64 v[54:57], v53 offset0:168 offset1:170
	s_waitcnt lgkmcnt(0)
	v_mfma_f32_32x32x16_bf16 v[4:19], v[54:57], v[40:43], v[4:19]
	ds_read2_b64 v[54:57], v58 offset0:140 offset1:142
	s_waitcnt lgkmcnt(0)
	v_mfma_f32_32x32x16_bf16 v[20:35], v[54:57], v[36:39], v[20:35]
	ds_read2_b64 v[54:57], v53 offset0:172 offset1:174
	s_waitcnt lgkmcnt(0)
	v_mfma_f32_32x32x16_bf16 v[4:19], v[54:57], v[36:39], v[4:19]
	s_branch .LBB0_848
